# final6 + last key-chunk's 4 PV MFMAs of step t deferred across the end-of-step barrier, issued at the head of step t+1 right after the K-fragment LDS reads; flushed on skip path and loop exit
# speedup vs baseline: 1.0019x; 1.0019x over previous
; DI int at_v_rd_base(int lane) { return ((lane & 3) << 3) | (((lane >> 2) & 3) << 6) | (((lane >> 4) & 1) << 5) | (((lane >> 5) & 1) << 8); }
; DI void attn_unit_diff(const Ctx& C, int l, int b, int h, int j) {
;     ...
;     f32x16 o[4], ol = {}; float m_run = 0.f; bool first = true;
; #pragma unroll
;     for (int d0 = 0; d0 < 4; ++d0) o[d0] = f32x16{};
;     const bf16x8 ones = {16256, 16256, 16256, 16256, 16256, 16256, 16256, 16256};
;     asm volatile("s_waitcnt vmcnt(0) lgkmcnt(0)\n\ts_barrier" ::: "memory");
;     const float cfar = tabl[0];
;     const int vrd = at_v_rd_base(lane);
;     for (int sd = 0; sd < nt; ++sd) {
;         const int slot = sd % 3;
;         const bool staged = sd + 2 < nt;
;         if (staged) at_stage1(C.lds, projb, kcolB, vcolB, sd + 2, (sd + 2) % 3, wid, lb0, lb1);
.LBB0_785:
	s_or_b64 exec, exec, s[38:39]
	s_add_i32 s50, 0, 0x20000
	s_lshr_b32 s28, s97, 4
	s_lshl_b32 s66, s49, 1
	v_readlane_b32 s38, v252, 22
	s_waitcnt vmcnt(0) lgkmcnt(0)
	s_barrier
	v_mov_b32_e32 v4, s50
	s_and_b32 s28, s28, 7
	s_or_b32 s67, s66, s38
	s_waitcnt lgkmcnt(0)
	ds_read_b32 v158, v4
	v_and_b32_e32 v4, 24, v8
	v_and_b32_e32 v7, 0x100, v8
	v_lshlrev_b32_e32 v8, 4, v156
	v_readlane_b32 s38, v252, 26
	s_lshl_b32 s28, s28, 8
	v_lshlrev_b32_e32 v145, 4, v154
	v_add_u32_e32 v9, s38, v8
	v_readlane_b32 s38, v252, 23
	v_lshlrev_b32_e32 v11, 4, v155
	v_lshlrev_b32_e32 v15, 2, v154
	s_add_i32 s88, s55, 0xfffffe90
	s_add_i32 s38, s38, s52
	s_add_i32 s91, 0, 0x4000
	s_add_i32 s52, s48, s28
	v_mov_b32_e32 v3, v1
	v_and_b32_e32 v5, 0xc0, v145
	v_lshlrev_b32_e32 v6, 1, v154
	v_lshlrev_b32_e32 v10, 8, v155
	v_and_b32_e32 v11, 0x70, v11
	v_add_u32_e32 v14, 0x60, v9
	v_xor_b32_e32 v157, 0x80, v15
	v_add_lshl_u32 v15, s38, v155, 2
	s_add_u32 s38, s96, s42
	v_and_b32_e32 v6, 32, v6
	v_add_u32_e32 v12, 32, v9
	v_add_u32_e32 v13, 64, v9
	v_sub_u32_e32 v159, v8, v15
	v_add3_u32 v5, v7, s91, v5
	v_xad_u32 v164, v14, v11, v10
	v_lshl_add_u64 v[2:3], s[42:43], 0, v[2:3]
	s_addc_u32 s39, s89, s43
	v_mov_b32_e32 v14, v1
	v_mov_b32_e32 v15, v1
	v_add3_u32 v160, v5, v6, v4
	v_xad_u32 v161, v9, v11, v10
	v_xad_u32 v162, v12, v11, v10
	v_xad_u32 v163, v13, v11, v10
	v_lshl_add_u64 v[146:147], s[70:71], 0, v[2:3]
	v_lshl_add_u64 v[148:149], s[72:73], 0, v[2:3]
	v_lshl_add_u64 v[150:151], s[38:39], 0, v[0:1]
	s_lshl_b32 s95, s49, 16
	v_mov_b32_e32 v0, v1
	v_mov_b32_e32 v2, v1
	v_mov_b32_e32 v3, v1
	v_mov_b32_e32 v4, v1
	v_mov_b32_e32 v5, v1
	v_mov_b32_e32 v6, v1
	v_mov_b32_e32 v7, v1
	v_mov_b32_e32 v8, v1
	v_mov_b32_e32 v9, v1
	v_mov_b32_e32 v10, v1
	v_mov_b32_e32 v11, v1
	v_mov_b32_e32 v12, v1
	v_mov_b32_e32 v13, v1
	v_mov_b64_e32 v[78:79], v[14:15]
	v_mov_b64_e32 v[62:63], v[14:15]
	v_mov_b64_e32 v[46:47], v[14:15]
	v_mov_b64_e32 v[30:31], v[14:15]
	v_mov_b64_e32 v[94:95], v[14:15]
	s_mov_b32 s79, 2
	s_add_i32 s95, s95, 0x10000
	s_mov_b32 s48, 0
	v_mov_b32_e32 v165, 0
	s_mov_b64 s[38:39], -1
	s_mov_b32 s49, 0
	v_mov_b64_e32 v[76:77], v[12:13]
	v_mov_b64_e32 v[74:75], v[10:11]
	v_mov_b64_e32 v[72:73], v[8:9]
	v_mov_b64_e32 v[70:71], v[6:7]
	v_mov_b64_e32 v[68:69], v[4:5]
	v_mov_b64_e32 v[66:67], v[2:3]
	v_mov_b64_e32 v[64:65], v[0:1]
	v_mov_b64_e32 v[60:61], v[12:13]
	v_mov_b64_e32 v[58:59], v[10:11]
	v_mov_b64_e32 v[56:57], v[8:9]
	v_mov_b64_e32 v[54:55], v[6:7]
	v_mov_b64_e32 v[52:53], v[4:5]
	v_mov_b64_e32 v[50:51], v[2:3]
	v_mov_b64_e32 v[48:49], v[0:1]
	v_mov_b64_e32 v[44:45], v[12:13]
	v_mov_b64_e32 v[42:43], v[10:11]
	v_mov_b64_e32 v[40:41], v[8:9]
	v_mov_b64_e32 v[38:39], v[6:7]
	v_mov_b64_e32 v[36:37], v[4:5]
	v_mov_b64_e32 v[34:35], v[2:3]
	v_mov_b64_e32 v[32:33], v[0:1]
	v_mov_b64_e32 v[28:29], v[12:13]
	v_mov_b64_e32 v[26:27], v[10:11]
	v_mov_b64_e32 v[24:25], v[8:9]
	v_mov_b64_e32 v[22:23], v[6:7]
	v_mov_b64_e32 v[20:21], v[4:5]
	v_mov_b64_e32 v[18:19], v[2:3]
	v_mov_b64_e32 v[16:17], v[0:1]
	v_mov_b64_e32 v[92:93], v[12:13]
	v_mov_b64_e32 v[90:91], v[10:11]
	v_mov_b64_e32 v[88:89], v[8:9]
	v_mov_b64_e32 v[86:87], v[6:7]
	v_mov_b64_e32 v[84:85], v[4:5]
	v_mov_b64_e32 v[82:83], v[2:3]
	v_mov_b64_e32 v[80:81], v[0:1]
	s_mov_b32 s94, 0
	s_waitcnt vmcnt(0)
	v_mov_b32_e32 v166, 0
	v_mov_b32_e32 v167, 0
	v_mov_b32_e32 v168, 0
	v_mov_b32_e32 v169, 0
	v_mov_b32_e32 v112, 0
	v_mov_b32_e32 v113, 0
	v_mov_b32_e32 v114, 0
	v_mov_b32_e32 v115, 0
	v_mov_b32_e32 v116, 0
	v_mov_b32_e32 v117, 0
	v_mov_b32_e32 v118, 0
	v_mov_b32_e32 v119, 0
	v_mov_b32_e32 v88, 0
	v_mov_b32_e32 v89, 0
	v_mov_b32_e32 v90, 0
	v_mov_b32_e32 v91, 0
	v_mov_b32_e32 v92, 0
	v_mov_b32_e32 v93, 0
	v_mov_b32_e32 v94, 0
	v_mov_b32_e32 v95, 0
	s_branch .LBB0_787

; #define LAS __attribute__((address_space(3)))
; #define MFMA32(a, b, c) __builtin_amdgcn_mfma_f32_32x32x16_bf16((a), (b), (c), 0, 0, 0)
; DI void attn_unit_diff(const Ctx& C, int l, int b, int h, int j) {
;     ...
;         if (sd <= cw) {
;             LAS const unsigned char* Kt = C.lds + slot * 32768;
;             const int vb = (int)(size_t)(Kt + 16384) + vrd;
;             const bool nearb = (sd * 64 + 63 - q0w) > -305;
;             LAS const float* tabp = tabl + (sd * 64 - qpos + TABB_OFF + 4 * hi);
;             f32x16 p0, p1;
;             at_qk<KS>(p0, p1, Kt, g * 128, qr, (nearb ? 0.f : cfar) - m_run, r32, hi);
;             const float alpha = at_softmax(p0, p1, m_run, first, nearb, tabp, lane);
;             first = false;
;             if (__any(alpha != 1.f)) {
;                 ol[0] *= alpha;
; #pragma unroll
;                 for (int d0 = 0; d0 < 4; ++d0)
; #pragma unroll
;                     for (int i = 0; i < 16; ++i) o[d0][i] *= alpha;
;             }
;             bf16x8 pf[4];
;             pf[0] = at_pack(p0, 0); pf[1] = at_pack(p0, 8); pf[2] = at_pack(p1, 0); pf[3] = at_pack(p1, 8);
;             ol = MFMA32(ones, pf[0], ol); ol = MFMA32(ones, pf[1], ol); ol = MFMA32(ones, pf[2], ol); ol = MFMA32(ones, pf[3], ol);
;             at_pv_block<0>(o, vb, pf); at_pv_block<1>(o, vb, pf); at_pv_block<2>(o, vb, pf); at_pv_block<3>(o, vb, pf);
;         }
;         if (staged) asm volatile("s_waitcnt vmcnt(4) lgkmcnt(0)\n\ts_barrier" ::: "memory");
.LBB0_789:
	v_mfma_f32_32x32x16_bf16 v[64:79], v[112:115], v[166:169], v[64:79]
	v_mfma_f32_32x32x16_bf16 v[48:63], v[116:119], v[166:169], v[48:63]
	v_mfma_f32_32x32x16_bf16 v[32:47], v[88:91], v[166:169], v[32:47]
	v_mfma_f32_32x32x16_bf16 v[16:31], v[92:95], v[166:169], v[16:31]
	s_nop 15
	v_mov_b32_e32 v166, 0
	v_mov_b32_e32 v167, 0
	v_mov_b32_e32 v168, 0
	v_mov_b32_e32 v169, 0
	s_mov_b64 s[58:59], -1
	s_and_b64 vcc, exec, s[40:41]
	s_cbranch_vccnz .LBB0_802

; #define LAS __attribute__((address_space(3)))
; #define MFMA32(a, b, c) __builtin_amdgcn_mfma_f32_32x32x16_bf16((a), (b), (c), 0, 0, 0)
;     __device__ __forceinline__ void init(const void* A_, const void* B_, int lda_, int ldb_, int M, unsigned mask_, int G_, int c_) { A = (const char*)A_; B = (const char*)B_; lda = lda_; ldb = ldb_; nM = M / BM; mask = mask_; nN = __builtin_popcount(mask_); nwg = nM * nN; G = G_; c = c_; }
;     __device__ __forceinline__ void init(f32x4 (&acc)[2][2][4][2], const Unit& u, int wr, int wc, int fr, int fq) const { u32x4 old[2][4][2]; init_load(old, u, wr, wc, fr, fq); init_finish(acc, old); }
; template <int KS> DI void at_qk(f32x16& p0, f32x16& p1, LAS const unsigned char* Kt, int mapB, const bf16x8 (&qr)[8], float init, int r32, int hi) {
; #pragma unroll
;     for (int i = 0; i < 16; ++i) { p0[i] = init; p1[i] = init; }
;     bf16x8 kb[KS][2];
; #pragma unroll
;     for (int d0 = 0; d0 < KS; ++d0) { const int cb = mapB + (d0 * 16 + hi * 8) * 2;
;         kb[d0][0] = *(const LAS bf16x8*)(Kt + AT_KSWZ(r32, cb)); kb[d0][1] = *(const LAS bf16x8*)(Kt + AT_KSWZ(32 + r32, cb)); }
;     __builtin_amdgcn_sched_barrier(0);
; #pragma unroll
;     for (int d0 = 0; d0 < KS; ++d0) { p0 = MFMA32(kb[d0][0], qr[d0], p0); p1 = MFMA32(kb[d0][1], qr[d0], p1); }
; DI void attn_unit_diff(const Ctx& C, int l, int b, int h, int j) {
;     ...
;         if (sd <= cw) {
;             LAS const unsigned char* Kt = C.lds + slot * 32768;
;             const int vb = (int)(size_t)(Kt + 16384) + vrd;
;             const bool nearb = (sd * 64 + 63 - q0w) > -305;
;             LAS const float* tabp = tabl + (sd * 64 - qpos + TABB_OFF + 4 * hi);
;             f32x16 p0, p1;
;             at_qk<KS>(p0, p1, Kt, g * 128, qr, (nearb ? 0.f : cfar) - m_run, r32, hi);
;             const float alpha = at_softmax(p0, p1, m_run, first, nearb, tabp, lane);
.LBB0_792:
	s_mul_hi_u32 s57, s94, 0xaaaaaaab
	s_lshr_b32 s57, s57, 1
	s_mul_i32 s57, s57, 0x18000
	s_cmp_le_u32 s48, s88
	v_subrev_u32_e32 v0, s57, v161
	s_cselect_b64 vcc, -1, 0
	s_add_i32 s58, s49, 0
	v_subrev_u32_e32 v10, s57, v162
	s_waitcnt lgkmcnt(0)
	v_cndmask_b32_e32 v2, 0, v158, vcc
	v_add_u32_e32 v0, s58, v0
	v_subrev_u32_e32 v14, s57, v163
	v_sub_f32_e32 v96, v2, v165
	ds_read_b128 v[2:5], v0
	ds_read_b128 v[6:9], v0 offset:8192
	v_add_u32_e32 v0, s58, v10
	v_subrev_u32_e32 v15, s57, v164
	ds_read_b128 v[10:13], v0
	ds_read_b128 v[186:189], v0 offset:8192
	v_add_u32_e32 v0, s58, v14
	ds_read_b128 v[170:173], v0
	ds_read_b128 v[174:177], v0 offset:8192
	v_add_u32_e32 v0, s58, v15
	ds_read_b128 v[178:181], v0
	ds_read_b128 v[182:185], v0 offset:8192
	v_mfma_f32_32x32x16_bf16 v[64:79], v[112:115], v[166:169], v[64:79]
	v_mfma_f32_32x32x16_bf16 v[48:63], v[116:119], v[166:169], v[48:63]
	v_mfma_f32_32x32x16_bf16 v[32:47], v[88:91], v[166:169], v[32:47]
	v_mfma_f32_32x32x16_bf16 v[16:31], v[92:95], v[166:169], v[16:31]
	v_mov_b32_e32 v97, v96
	v_mov_b32_e32 v98, v96
	v_mov_b32_e32 v99, v96
	v_mov_b32_e32 v100, v96
	v_mov_b32_e32 v101, v96
	v_mov_b32_e32 v102, v96
	v_mov_b32_e32 v103, v96
	v_mov_b32_e32 v104, v96
	v_mov_b32_e32 v105, v96
	v_mov_b32_e32 v106, v96
	v_mov_b32_e32 v107, v96
	v_mov_b32_e32 v108, v96
	v_mov_b32_e32 v109, v96
	v_mov_b32_e32 v110, v96
	v_mov_b32_e32 v111, v96
	s_waitcnt lgkmcnt(0)
	s_nop 0
	v_mfma_f32_32x32x16_bf16 v[112:127], v[2:5], v[128:131], v[96:111]
	s_and_b64 vcc, exec, vcc
	v_mfma_f32_32x32x16_bf16 v[96:111], v[6:9], v[128:131], v[96:111]
	v_mfma_f32_32x32x16_bf16 v[112:127], v[10:13], v[132:135], v[112:127]
	v_mfma_f32_32x32x16_bf16 v[96:111], v[186:189], v[132:135], v[96:111]
	v_mfma_f32_32x32x16_bf16 v[112:127], v[170:173], v[136:139], v[112:127]
	v_mfma_f32_32x32x16_bf16 v[96:111], v[174:177], v[136:139], v[96:111]
	v_mfma_f32_32x32x16_bf16 v[112:127], v[178:181], v[140:143], v[112:127]
	v_mfma_f32_32x32x16_bf16 v[96:111], v[182:185], v[140:143], v[96:111]
	s_cbranch_vccnz .LBB0_794
	v_add_u32_e32 v0, 0, v159
	v_add_u32_e32 v2, 0x207fc, v0
	v_add_u32_e32 v4, 0x2087c, v0
	ds_read2_b32 v[2:3], v2 offset1:1
	ds_read2_b32 v[4:5], v4 offset1:1
	v_add_u32_e32 v6, 0x20804, v0
	v_add_u32_e32 v8, 0x20884, v0
	v_add_u32_e32 v10, 0x2081c, v0
	v_add_u32_e32 v12, 0x2089c, v0
	v_add_u32_e32 v14, 0x20824, v0
	v_add_u32_e32 v166, 0x208a4, v0
	v_add_u32_e32 v168, 0x2083c, v0
	v_add_u32_e32 v170, 0x208bc, v0
	v_add_u32_e32 v172, 0x20844, v0
	v_add_u32_e32 v174, 0x208c4, v0
	v_add_u32_e32 v176, 0x2085c, v0
	v_add_u32_e32 v178, 0x208dc, v0
	v_add_u32_e32 v180, 0x20864, v0
	v_add_u32_e32 v0, 0x208e4, v0
	ds_read2_b32 v[6:7], v6 offset1:1
	ds_read2_b32 v[8:9], v8 offset1:1
	ds_read2_b32 v[10:11], v10 offset1:1
	ds_read2_b32 v[12:13], v12 offset1:1
	ds_read2_b32 v[14:15], v14 offset1:1
	ds_read2_b32 v[166:167], v166 offset1:1
	ds_read2_b32 v[168:169], v168 offset1:1
	ds_read2_b32 v[170:171], v170 offset1:1
	ds_read2_b32 v[172:173], v172 offset1:1
	ds_read2_b32 v[174:175], v174 offset1:1
	ds_read2_b32 v[176:177], v176 offset1:1
	ds_read2_b32 v[178:179], v178 offset1:1
	ds_read2_b32 v[180:181], v180 offset1:1
	s_waitcnt lgkmcnt(0)
	v_pk_add_f32 v[112:113], v[112:113], v[2:3]
	ds_read2_b32 v[2:3], v0 offset1:1
	v_pk_add_f32 v[124:125], v[124:125], v[176:177]
	v_pk_add_f32 v[122:123], v[122:123], v[172:173]
	v_pk_add_f32 v[126:127], v[126:127], v[180:181]
	v_pk_add_f32 v[120:121], v[120:121], v[168:169]
	v_pk_add_f32 v[118:119], v[118:119], v[14:15]
	v_pk_add_f32 v[116:117], v[116:117], v[10:11]
	v_pk_add_f32 v[114:115], v[114:115], v[6:7]
	s_waitcnt lgkmcnt(0)
	v_pk_add_f32 v[110:111], v[110:111], v[2:3]
	v_pk_add_f32 v[108:109], v[108:109], v[178:179]
	v_pk_add_f32 v[106:107], v[106:107], v[174:175]
	v_pk_add_f32 v[104:105], v[104:105], v[170:171]
	v_pk_add_f32 v[102:103], v[102:103], v[166:167]
	v_pk_add_f32 v[100:101], v[100:101], v[12:13]
	v_pk_add_f32 v[98:99], v[98:99], v[8:9]
	v_pk_add_f32 v[96:97], v[96:97], v[4:5]

; #define MFMA32(a, b, c) __builtin_amdgcn_mfma_f32_32x32x16_bf16((a), (b), (c), 0, 0, 0)
; template <int OFF> DI s16x4 at_tr_read(int vb) { s16x4 r; asm volatile("ds_read_b64_tr_b16 %0, %1 offset:%2" : "=&v"(r) : "v"(vb), "i"(OFF) : "memory"); return r; }
; DI unsigned at_cvtpk(float lo, float hi) { unsigned r; asm volatile("v_cvt_pk_bf16_f32 %0, %1, %2" : "=v"(r) : "v"(lo), "v"(hi)); return r; }
; DI float at_softmax(f32x16& p0, f32x16& p1, float& m_run, bool first, bool nearb, LAS const float* tabp, int lane) {
;     ...
;     for (int i = 0; i < 16; ++i) p0[i] = __builtin_amdgcn_exp2f(p0[i]);
; #pragma unroll
;     for (int i = 0; i < 16; ++i) p1[i] = __builtin_amdgcn_exp2f(p1[i]);
;     return alpha;
; }
; DI bf16x8 at_pack(const f32x16& p, int s8) {
;     u32x4 w; w.x = at_cvtpk(p[s8], p[s8 + 1]); w.y = at_cvtpk(p[s8 + 2], p[s8 + 3]); w.z = at_cvtpk(p[s8 + 4], p[s8 + 5]); w.w = at_cvtpk(p[s8 + 6], p[s8 + 7]);
;     return __builtin_bit_cast(bf16x8, w);
; }
; template <int D0> DI void at_pv_block(f32x16 (&o)[4], int vb, const bf16x8 (&pf)[4]) {
;     const s16x4 l0 = at_tr_read<D0 * 512 + 0 * 4096>(vb), h0 = at_tr_read<D0 * 512 + 0 * 4096 + 2048>(vb), l1 = at_tr_read<D0 * 512 + 1 * 4096>(vb), h1 = at_tr_read<D0 * 512 + 1 * 4096 + 2048>(vb);
;     const s16x4 l2 = at_tr_read<D0 * 512 + 2 * 4096>(vb), h2 = at_tr_read<D0 * 512 + 2 * 4096 + 2048>(vb), l3 = at_tr_read<D0 * 512 + 3 * 4096>(vb), h3 = at_tr_read<D0 * 512 + 3 * 4096 + 2048>(vb);
;     asm volatile("s_waitcnt lgkmcnt(0)" ::: "memory"); __builtin_amdgcn_sched_barrier(0);
;     ...
;     o[D0] = MFMA32(AT_PK(l0, h0), pf[0], o[D0]); o[D0] = MFMA32(AT_PK(l1, h1), pf[1], o[D0]); o[D0] = MFMA32(AT_PK(l2, h2), pf[2], o[D0]); o[D0] = MFMA32(AT_PK(l3, h3), pf[3], o[D0]);
; DI void attn_unit_diff(const Ctx& C, int l, int b, int h, int j) {
;     ...
;             pf[0] = at_pack(p0, 0); pf[1] = at_pack(p0, 8); pf[2] = at_pack(p1, 0); pf[3] = at_pack(p1, 8);
;             ol = MFMA32(ones, pf[0], ol); ol = MFMA32(ones, pf[1], ol); ol = MFMA32(ones, pf[2], ol); ol = MFMA32(ones, pf[3], ol);
;             at_pv_block<0>(o, vb, pf); at_pv_block<1>(o, vb, pf); at_pv_block<2>(o, vb, pf); at_pv_block<3>(o, vb, pf);
.LBB0_801:
	v_subrev_u32_e32 v87, s57, v160
	v_add_u32_e32 v87, s49, v87
	ds_read_b64_tr_b16 v[170:171], v87 offset:0x0
	ds_read_b64_tr_b16 v[172:173], v87 offset:0x800
	ds_read_b64_tr_b16 v[174:175], v87 offset:0x200
	ds_read_b64_tr_b16 v[176:177], v87 offset:0xa00
	ds_read_b64_tr_b16 v[178:179], v87 offset:0x400
	ds_read_b64_tr_b16 v[180:181], v87 offset:0xc00
	ds_read_b64_tr_b16 v[182:183], v87 offset:0x600
	ds_read_b64_tr_b16 v[184:185], v87 offset:0xe00
	v_exp_f32_e32 v112, v112
	v_exp_f32_e32 v113, v113
	v_exp_f32_e32 v114, v114
	v_exp_f32_e32 v115, v115
	v_exp_f32_e32 v116, v116
	v_exp_f32_e32 v117, v117
	v_exp_f32_e32 v118, v118
	v_exp_f32_e32 v119, v119
	v_cvt_pk_bf16_f32 v2, v112, v113
	v_cvt_pk_bf16_f32 v3, v114, v115
	v_cvt_pk_bf16_f32 v4, v116, v117
	v_cvt_pk_bf16_f32 v5, v118, v119
	v_add_f32_e32 v81, v112, v113
	v_add_f32_e32 v82, v114, v115
	v_add_f32_e32 v83, v116, v117
	v_add_f32_e32 v84, v118, v119
	v_add_f32_e32 v81, v81, v82
	v_add_f32_e32 v83, v83, v84
	v_add_f32_e32 v81, v81, v83
	v_add_f32_e32 v80, v80, v81
	s_waitcnt lgkmcnt(0)
	ds_read_b64_tr_b16 v[112:113], v87 offset:0x1000
	ds_read_b64_tr_b16 v[114:115], v87 offset:0x1800
	ds_read_b64_tr_b16 v[116:117], v87 offset:0x1200
	ds_read_b64_tr_b16 v[118:119], v87 offset:0x1a00
	ds_read_b64_tr_b16 v[88:89], v87 offset:0x1400
	ds_read_b64_tr_b16 v[90:91], v87 offset:0x1c00
	ds_read_b64_tr_b16 v[92:93], v87 offset:0x1600
	ds_read_b64_tr_b16 v[94:95], v87 offset:0x1e00
	v_mfma_f32_32x32x16_bf16 v[64:79], v[170:173], v[2:5], v[64:79]
	v_exp_f32_e32 v120, v120
	v_exp_f32_e32 v121, v121
	v_mfma_f32_32x32x16_bf16 v[48:63], v[174:177], v[2:5], v[48:63]
	v_exp_f32_e32 v122, v122
	v_exp_f32_e32 v123, v123
	v_mfma_f32_32x32x16_bf16 v[32:47], v[178:181], v[2:5], v[32:47]
	v_exp_f32_e32 v124, v124
	v_exp_f32_e32 v125, v125
	v_mfma_f32_32x32x16_bf16 v[16:31], v[182:185], v[2:5], v[16:31]
	v_exp_f32_e32 v126, v126
	v_exp_f32_e32 v127, v127
	v_cvt_pk_bf16_f32 v6, v120, v121
	v_cvt_pk_bf16_f32 v7, v122, v123
	v_cvt_pk_bf16_f32 v8, v124, v125
	v_cvt_pk_bf16_f32 v9, v126, v127
	v_add_f32_e32 v81, v120, v121
	v_add_f32_e32 v82, v122, v123
	v_add_f32_e32 v83, v124, v125
	v_add_f32_e32 v84, v126, v127
	v_add_f32_e32 v81, v81, v82
	v_add_f32_e32 v83, v83, v84
	v_add_f32_e32 v81, v81, v83
	v_add_f32_e32 v80, v80, v81
	s_waitcnt lgkmcnt(0)
	ds_read_b64_tr_b16 v[170:171], v87 offset:0x2000
	ds_read_b64_tr_b16 v[172:173], v87 offset:0x2800
	ds_read_b64_tr_b16 v[174:175], v87 offset:0x2200
	ds_read_b64_tr_b16 v[176:177], v87 offset:0x2a00
	ds_read_b64_tr_b16 v[178:179], v87 offset:0x2400
	ds_read_b64_tr_b16 v[180:181], v87 offset:0x2c00
	ds_read_b64_tr_b16 v[182:183], v87 offset:0x2600
	ds_read_b64_tr_b16 v[184:185], v87 offset:0x2e00
	v_mfma_f32_32x32x16_bf16 v[64:79], v[112:115], v[6:9], v[64:79]
	v_exp_f32_e32 v96, v96
	v_exp_f32_e32 v97, v97
	v_mfma_f32_32x32x16_bf16 v[48:63], v[116:119], v[6:9], v[48:63]
	v_exp_f32_e32 v98, v98
	v_exp_f32_e32 v99, v99
	v_mfma_f32_32x32x16_bf16 v[32:47], v[88:91], v[6:9], v[32:47]
	v_exp_f32_e32 v100, v100
	v_exp_f32_e32 v101, v101
	v_mfma_f32_32x32x16_bf16 v[16:31], v[92:95], v[6:9], v[16:31]
	v_exp_f32_e32 v102, v102
	v_exp_f32_e32 v103, v103
	v_cvt_pk_bf16_f32 v10, v96, v97
	v_cvt_pk_bf16_f32 v11, v98, v99
	v_cvt_pk_bf16_f32 v12, v100, v101
	v_cvt_pk_bf16_f32 v13, v102, v103
	v_add_f32_e32 v81, v96, v97
	v_add_f32_e32 v82, v98, v99
	v_add_f32_e32 v83, v100, v101
	v_add_f32_e32 v84, v102, v103
	v_add_f32_e32 v81, v81, v82
	v_add_f32_e32 v83, v83, v84
	v_add_f32_e32 v81, v81, v83
	v_add_f32_e32 v80, v80, v81
	s_waitcnt lgkmcnt(0)
	ds_read_b64_tr_b16 v[112:113], v87 offset:0x3000
	ds_read_b64_tr_b16 v[114:115], v87 offset:0x3800
	ds_read_b64_tr_b16 v[116:117], v87 offset:0x3200
	ds_read_b64_tr_b16 v[118:119], v87 offset:0x3a00
	ds_read_b64_tr_b16 v[88:89], v87 offset:0x3400
	ds_read_b64_tr_b16 v[90:91], v87 offset:0x3c00
	ds_read_b64_tr_b16 v[92:93], v87 offset:0x3600
	ds_read_b64_tr_b16 v[94:95], v87 offset:0x3e00
	v_mfma_f32_32x32x16_bf16 v[64:79], v[170:173], v[10:13], v[64:79]
	v_exp_f32_e32 v104, v104
	v_exp_f32_e32 v105, v105
	v_mfma_f32_32x32x16_bf16 v[48:63], v[174:177], v[10:13], v[48:63]
	v_exp_f32_e32 v106, v106
	v_exp_f32_e32 v107, v107
	v_mfma_f32_32x32x16_bf16 v[32:47], v[178:181], v[10:13], v[32:47]
	v_exp_f32_e32 v108, v108
	v_exp_f32_e32 v109, v109
	v_mfma_f32_32x32x16_bf16 v[16:31], v[182:185], v[10:13], v[16:31]
	v_exp_f32_e32 v110, v110
	v_exp_f32_e32 v111, v111
	v_cvt_pk_bf16_f32 v166, v104, v105
	v_cvt_pk_bf16_f32 v167, v106, v107
	v_cvt_pk_bf16_f32 v168, v108, v109
	v_cvt_pk_bf16_f32 v169, v110, v111
	v_add_f32_e32 v81, v104, v105
	v_add_f32_e32 v82, v106, v107
	v_add_f32_e32 v83, v108, v109
	v_add_f32_e32 v84, v110, v111
	v_add_f32_e32 v81, v81, v82
	v_add_f32_e32 v83, v83, v84
	v_add_f32_e32 v81, v81, v83
	v_add_f32_e32 v80, v80, v81
	s_waitcnt lgkmcnt(0)
	s_mov_b64 s[38:39], 0
	s_mov_b64 s[58:59], -1
	s_and_b64 vcc, exec, s[40:41]
	s_cbranch_vccz .LBB0_790

; #define LAS __attribute__((address_space(3)))
; #define CIN(i) ((const float*)*(const GAS float* const __attribute__((address_space(4)))*)(C.ka + 8 * (i)))
; DI void attn_unit_diff(const Ctx& C, int l, int b, int h, int j) {
;     ...
;     const float inv = 1.f / ol[0];
;     LAS float* cmb = (LAS float*)C.lds + (size_t)wq * (64 * 64);
;     f32x4 sgv[4][4];
;     if (g == 0) { const float* sg0 = CIN(I_SUBLN) + l * 128;
; #pragma unroll
;         for (int d0 = 0; d0 < 4; ++d0)
; #pragma unroll
;             for (int gq = 0; gq < 4; ++gq) sgv[d0][gq] = *(const f32x4*)(sg0 + 32 * d0 + 8 * gq + 4 * hi); }
.LBB0_805:
	v_mfma_f32_32x32x16_bf16 v[64:79], v[112:115], v[166:169], v[64:79]
	v_mfma_f32_32x32x16_bf16 v[48:63], v[116:119], v[166:169], v[48:63]
	v_mfma_f32_32x32x16_bf16 v[32:47], v[88:91], v[166:169], v[32:47]
	v_mfma_f32_32x32x16_bf16 v[16:31], v[92:95], v[166:169], v[16:31]
	s_nop 15
v_lshlrev_b32_e32 v81, 2, v154
v_xor_b32_e32 v81, 0x80, v81
ds_bpermute_b32 v82, v81, v80
s_waitcnt lgkmcnt(0)
v_add_f32_e32 v80, v80, v82
	v_readlane_b32 s38, v252, 27
	v_readlane_b32 s39, v252, 28
	s_and_b64 vcc, s[38:39], exec
	s_cbranch_vccz .LBB0_807
	s_load_dwordx2 s[38:39], s[0:1], 0x38
	v_readlane_b32 s40, v254, 25
	v_readlane_b32 s41, v254, 26
	s_lshl_b64 s[40:41], s[40:41], 2
	v_lshlrev_b32_e32 v2, 2, v156
	s_waitcnt lgkmcnt(0)
	s_add_u32 s38, s38, s40
	v_ashrrev_i32_e32 v3, 31, v2
	s_addc_u32 s39, s39, s41
	v_lshl_add_u64 v[2:3], v[2:3], 2, s[38:39]
	global_load_dwordx4 v[126:129], v[2:3], off
	global_load_dwordx4 v[94:97], v[2:3], off offset:32
	global_load_dwordx4 v[86:89], v[2:3], off offset:64
	global_load_dwordx4 v[82:85], v[2:3], off offset:96
	global_load_dwordx4 v[90:93], v[2:3], off offset:128
	global_load_dwordx4 v[98:101], v[2:3], off offset:160
	global_load_dwordx4 v[102:105], v[2:3], off offset:192
	global_load_dwordx4 v[106:109], v[2:3], off offset:224
	global_load_dwordx4 v[110:113], v[2:3], off offset:256
	global_load_dwordx4 v[114:117], v[2:3], off offset:288
	global_load_dwordx4 v[118:121], v[2:3], off offset:320
	global_load_dwordx4 v[122:125], v[2:3], off offset:352
	global_load_dwordx4 v[130:133], v[2:3], off offset:384
	global_load_dwordx4 v[10:13], v[2:3], off offset:416
	global_load_dwordx4 v[6:9], v[2:3], off offset:448
	s_nop 0
	global_load_dwordx4 v[2:5], v[2:3], off offset:480

; DI int at_v_rd_base(int lane) { return ((lane & 3) << 3) | (((lane >> 2) & 3) << 6) | (((lane >> 4) & 1) << 5) | (((lane >> 5) & 1) << 8); }
; DI void attn_unit_diff(const Ctx& C, int l, int b, int h, int j) {
;     ...
;     f32x16 o[4], ol = {}; float m_run = 0.f; bool first = true;
; #pragma unroll
;     for (int d0 = 0; d0 < 4; ++d0) o[d0] = f32x16{};
;     const bf16x8 ones = {16256, 16256, 16256, 16256, 16256, 16256, 16256, 16256};
;     asm volatile("s_waitcnt vmcnt(0) lgkmcnt(0)\n\ts_barrier" ::: "memory");
;     const float cfar = tabl[0];
;     const int vrd = at_v_rd_base(lane);
;     for (int sd = 0; sd < nt; ++sd) {
;         const int slot = sd % 3;
;         const bool staged = sd + 2 < nt;
;         if (staged) at_stage1(C.lds, projb, kcolB, vcolB, sd + 2, (sd + 2) % 3, wid, lb0, lb1);
.LBB0_828:
	s_or_b64 exec, exec, s[58:59]
	s_and_b32 s11, s22, 15
	s_waitcnt vmcnt(0) lgkmcnt(0)
	s_barrier
	v_mov_b32_e32 v4, s50
	s_lshl_b32 s6, s6, 1
	v_readlane_b32 s7, v252, 22
	s_lshl_b32 s31, s11, 7
	s_lshl_b32 s11, s11, 16
	s_waitcnt lgkmcnt(0)
	ds_read_b32 v158, v4
	v_and_b32_e32 v4, 24, v8
	v_and_b32_e32 v7, 0x100, v8
	v_lshlrev_b32_e32 v8, 4, v156
	v_readlane_b32 s15, v252, 26
	v_readlane_b32 s35, v252, 23
	v_mov_b32_e32 v3, v1
	s_or_b32 s7, s6, s7
	s_add_i32 s11, s11, 0x10000
	v_lshlrev_b32_e32 v145, 4, v154
	v_add_u32_e32 v9, s15, v8
	v_lshlrev_b32_e32 v11, 4, v155
	v_lshlrev_b32_e32 v15, 2, v154
	s_add_i32 s16, s55, 0xfffffe90
	s_or_b32 s31, s35, s31
	s_add_i32 s52, s48, s28
	v_and_b32_e32 v5, 0xc0, v145
	v_lshlrev_b32_e32 v6, 1, v154
	v_lshlrev_b32_e32 v10, 8, v155
	v_and_b32_e32 v11, 0x70, v11
	v_add_u32_e32 v14, 0x60, v9
	v_xor_b32_e32 v157, 0x80, v15
	v_add_lshl_u32 v15, s31, v155, 2
	v_lshl_add_u64 v[2:3], s[42:43], 0, v[2:3]
	s_add_u32 s42, s96, s42
	v_and_b32_e32 v6, 32, v6
	v_add_u32_e32 v12, 32, v9
	v_add_u32_e32 v13, 64, v9
	v_sub_u32_e32 v159, v8, v15
	v_add3_u32 v5, v7, s91, v5
	v_xad_u32 v164, v14, v11, v10
	s_addc_u32 s43, s89, s43
	v_mov_b32_e32 v14, v1
	v_mov_b32_e32 v15, v1
	v_add3_u32 v160, v5, v6, v4
	v_xad_u32 v161, v9, v11, v10
	v_xad_u32 v162, v12, v11, v10
	v_xad_u32 v163, v13, v11, v10
	v_lshl_add_u64 v[146:147], s[70:71], 0, v[2:3]
	v_lshl_add_u64 v[148:149], s[72:73], 0, v[2:3]
	v_lshl_add_u64 v[150:151], s[42:43], 0, v[0:1]
	v_mov_b32_e32 v0, v1
	v_mov_b32_e32 v2, v1
	v_mov_b32_e32 v3, v1
	v_mov_b32_e32 v4, v1
	v_mov_b32_e32 v5, v1
	v_mov_b32_e32 v6, v1
	v_mov_b32_e32 v7, v1
	v_mov_b32_e32 v8, v1
	v_mov_b32_e32 v9, v1
	v_mov_b32_e32 v10, v1
	v_mov_b32_e32 v11, v1
	v_mov_b32_e32 v12, v1
	v_mov_b32_e32 v13, v1
	v_mov_b64_e32 v[78:79], v[14:15]
	v_mov_b64_e32 v[62:63], v[14:15]
	v_mov_b64_e32 v[46:47], v[14:15]
	v_mov_b64_e32 v[30:31], v[14:15]
	v_mov_b64_e32 v[94:95], v[14:15]
	s_mov_b32 s15, 2
	s_mov_b32 s28, 0
	v_mov_b32_e32 v165, 0
	s_mov_b64 s[42:43], -1
	s_mov_b32 s31, 0
	v_mov_b64_e32 v[76:77], v[12:13]
	v_mov_b64_e32 v[74:75], v[10:11]
	v_mov_b64_e32 v[72:73], v[8:9]
	v_mov_b64_e32 v[70:71], v[6:7]
	v_mov_b64_e32 v[68:69], v[4:5]
	v_mov_b64_e32 v[66:67], v[2:3]
	v_mov_b64_e32 v[64:65], v[0:1]
	v_mov_b64_e32 v[60:61], v[12:13]
	v_mov_b64_e32 v[58:59], v[10:11]
	v_mov_b64_e32 v[56:57], v[8:9]
	v_mov_b64_e32 v[54:55], v[6:7]
	v_mov_b64_e32 v[52:53], v[4:5]
	v_mov_b64_e32 v[50:51], v[2:3]
	v_mov_b64_e32 v[48:49], v[0:1]
	v_mov_b64_e32 v[44:45], v[12:13]
	v_mov_b64_e32 v[42:43], v[10:11]
	v_mov_b64_e32 v[40:41], v[8:9]
	v_mov_b64_e32 v[38:39], v[6:7]
	v_mov_b64_e32 v[36:37], v[4:5]
	v_mov_b64_e32 v[34:35], v[2:3]
	v_mov_b64_e32 v[32:33], v[0:1]
	v_mov_b64_e32 v[28:29], v[12:13]
	v_mov_b64_e32 v[26:27], v[10:11]
	v_mov_b64_e32 v[24:25], v[8:9]
	v_mov_b64_e32 v[22:23], v[6:7]
	v_mov_b64_e32 v[20:21], v[4:5]
	v_mov_b64_e32 v[18:19], v[2:3]
	v_mov_b64_e32 v[16:17], v[0:1]
	v_mov_b64_e32 v[92:93], v[12:13]
	v_mov_b64_e32 v[90:91], v[10:11]
	v_mov_b64_e32 v[88:89], v[8:9]
	v_mov_b64_e32 v[86:87], v[6:7]
	v_mov_b64_e32 v[84:85], v[4:5]
	v_mov_b64_e32 v[82:83], v[2:3]
	v_mov_b64_e32 v[80:81], v[0:1]
	s_mov_b32 s35, 0
	s_waitcnt vmcnt(0)
	v_mov_b32_e32 v166, 0
	v_mov_b32_e32 v167, 0
	v_mov_b32_e32 v168, 0
	v_mov_b32_e32 v169, 0
	v_mov_b32_e32 v112, 0
	v_mov_b32_e32 v113, 0
	v_mov_b32_e32 v114, 0
	v_mov_b32_e32 v115, 0
	v_mov_b32_e32 v116, 0
	v_mov_b32_e32 v117, 0
	v_mov_b32_e32 v118, 0
	v_mov_b32_e32 v119, 0
	v_mov_b32_e32 v88, 0
	v_mov_b32_e32 v89, 0
	v_mov_b32_e32 v90, 0
	v_mov_b32_e32 v91, 0
	v_mov_b32_e32 v92, 0
	v_mov_b32_e32 v93, 0
	v_mov_b32_e32 v94, 0
	v_mov_b32_e32 v95, 0
	s_branch .LBB0_830

; #define LAS __attribute__((address_space(3)))
; #define MFMA32(a, b, c) __builtin_amdgcn_mfma_f32_32x32x16_bf16((a), (b), (c), 0, 0, 0)
; DI void attn_unit_diff(const Ctx& C, int l, int b, int h, int j) {
;     ...
;         if (sd <= cw) {
;             LAS const unsigned char* Kt = C.lds + slot * 32768;
;             const int vb = (int)(size_t)(Kt + 16384) + vrd;
;             const bool nearb = (sd * 64 + 63 - q0w) > -305;
;             LAS const float* tabp = tabl + (sd * 64 - qpos + TABB_OFF + 4 * hi);
;             f32x16 p0, p1;
;             at_qk<KS>(p0, p1, Kt, g * 128, qr, (nearb ? 0.f : cfar) - m_run, r32, hi);
;             const float alpha = at_softmax(p0, p1, m_run, first, nearb, tabp, lane);
;             first = false;
;             if (__any(alpha != 1.f)) {
;                 ol[0] *= alpha;
; #pragma unroll
;                 for (int d0 = 0; d0 < 4; ++d0)
; #pragma unroll
;                     for (int i = 0; i < 16; ++i) o[d0][i] *= alpha;
;             }
;             bf16x8 pf[4];
;             pf[0] = at_pack(p0, 0); pf[1] = at_pack(p0, 8); pf[2] = at_pack(p1, 0); pf[3] = at_pack(p1, 8);
;             ol = MFMA32(ones, pf[0], ol); ol = MFMA32(ones, pf[1], ol); ol = MFMA32(ones, pf[2], ol); ol = MFMA32(ones, pf[3], ol);
;             at_pv_block<0>(o, vb, pf); at_pv_block<1>(o, vb, pf); at_pv_block<2>(o, vb, pf); at_pv_block<3>(o, vb, pf);
;         }
;         if (staged) asm volatile("s_waitcnt vmcnt(4) lgkmcnt(0)\n\ts_barrier" ::: "memory");
.LBB0_832:
	v_mfma_f32_32x32x16_bf16 v[64:79], v[112:115], v[166:169], v[64:79]
	v_mfma_f32_32x32x16_bf16 v[48:63], v[116:119], v[166:169], v[48:63]
	v_mfma_f32_32x32x16_bf16 v[32:47], v[88:91], v[166:169], v[32:47]
	v_mfma_f32_32x32x16_bf16 v[16:31], v[92:95], v[166:169], v[16:31]
	s_nop 15
	v_mov_b32_e32 v166, 0
	v_mov_b32_e32 v167, 0
	v_mov_b32_e32 v168, 0
	v_mov_b32_e32 v169, 0
	s_mov_b64 s[58:59], -1
	s_and_b64 vcc, exec, s[76:77]
	s_cbranch_vccnz .LBB0_845

; #define LAS __attribute__((address_space(3)))
; #define MFMA32(a, b, c) __builtin_amdgcn_mfma_f32_32x32x16_bf16((a), (b), (c), 0, 0, 0)
;     __device__ __forceinline__ void init(const void* A_, const void* B_, int lda_, int ldb_, int M, unsigned mask_, int G_, int c_) { A = (const char*)A_; B = (const char*)B_; lda = lda_; ldb = ldb_; nM = M / BM; mask = mask_; nN = __builtin_popcount(mask_); nwg = nM * nN; G = G_; c = c_; }
;     __device__ __forceinline__ void init(f32x4 (&acc)[2][2][4][2], const Unit& u, int wr, int wc, int fr, int fq) const { u32x4 old[2][4][2]; init_load(old, u, wr, wc, fr, fq); init_finish(acc, old); }
; template <int KS> DI void at_qk(f32x16& p0, f32x16& p1, LAS const unsigned char* Kt, int mapB, const bf16x8 (&qr)[8], float init, int r32, int hi) {
; #pragma unroll
;     for (int i = 0; i < 16; ++i) { p0[i] = init; p1[i] = init; }
;     bf16x8 kb[KS][2];
; #pragma unroll
;     for (int d0 = 0; d0 < KS; ++d0) { const int cb = mapB + (d0 * 16 + hi * 8) * 2;
;         kb[d0][0] = *(const LAS bf16x8*)(Kt + AT_KSWZ(r32, cb)); kb[d0][1] = *(const LAS bf16x8*)(Kt + AT_KSWZ(32 + r32, cb)); }
;     __builtin_amdgcn_sched_barrier(0);
; #pragma unroll
;     for (int d0 = 0; d0 < KS; ++d0) { p0 = MFMA32(kb[d0][0], qr[d0], p0); p1 = MFMA32(kb[d0][1], qr[d0], p1); }
; DI void attn_unit_diff(const Ctx& C, int l, int b, int h, int j) {
;     ...
;         if (sd <= cw) {
;             LAS const unsigned char* Kt = C.lds + slot * 32768;
;             const int vb = (int)(size_t)(Kt + 16384) + vrd;
;             const bool nearb = (sd * 64 + 63 - q0w) > -305;
;             LAS const float* tabp = tabl + (sd * 64 - qpos + TABB_OFF + 4 * hi);
;             f32x16 p0, p1;
;             at_qk<KS>(p0, p1, Kt, g * 128, qr, (nearb ? 0.f : cfar) - m_run, r32, hi);
;             const float alpha = at_softmax(p0, p1, m_run, first, nearb, tabp, lane);
.LBB0_835:
	s_mul_hi_u32 s48, s35, 0xaaaaaaab
	s_lshr_b32 s48, s48, 1
	s_mul_i32 s48, s48, 0x18000
	s_cmp_le_i32 s28, s16
	v_subrev_u32_e32 v0, s48, v161
	s_cselect_b64 vcc, -1, 0
	s_add_i32 s49, s31, 0
	v_subrev_u32_e32 v10, s48, v162
	s_waitcnt lgkmcnt(0)
	v_cndmask_b32_e32 v2, 0, v158, vcc
	v_add_u32_e32 v0, s49, v0
	v_subrev_u32_e32 v14, s48, v163
	v_sub_f32_e32 v96, v2, v165
	ds_read_b128 v[2:5], v0
	ds_read_b128 v[6:9], v0 offset:8192
	v_add_u32_e32 v0, s49, v10
	v_subrev_u32_e32 v15, s48, v164
	ds_read_b128 v[10:13], v0
	ds_read_b128 v[186:189], v0 offset:8192
	v_add_u32_e32 v0, s49, v14
	ds_read_b128 v[170:173], v0
	ds_read_b128 v[174:177], v0 offset:8192
	v_add_u32_e32 v0, s49, v15
	ds_read_b128 v[178:181], v0
	ds_read_b128 v[182:185], v0 offset:8192
	v_mfma_f32_32x32x16_bf16 v[64:79], v[112:115], v[166:169], v[64:79]
	v_mfma_f32_32x32x16_bf16 v[48:63], v[116:119], v[166:169], v[48:63]
	v_mfma_f32_32x32x16_bf16 v[32:47], v[88:91], v[166:169], v[32:47]
	v_mfma_f32_32x32x16_bf16 v[16:31], v[92:95], v[166:169], v[16:31]
	v_mov_b32_e32 v97, v96
	v_mov_b32_e32 v98, v96
	v_mov_b32_e32 v99, v96
	v_mov_b32_e32 v100, v96
	v_mov_b32_e32 v101, v96
	v_mov_b32_e32 v102, v96
	v_mov_b32_e32 v103, v96
	v_mov_b32_e32 v104, v96
	v_mov_b32_e32 v105, v96
	v_mov_b32_e32 v106, v96
	v_mov_b32_e32 v107, v96
	v_mov_b32_e32 v108, v96
	v_mov_b32_e32 v109, v96
	v_mov_b32_e32 v110, v96
	v_mov_b32_e32 v111, v96
	s_waitcnt lgkmcnt(0)
	s_nop 0
	v_mfma_f32_32x32x16_bf16 v[112:127], v[2:5], v[128:131], v[96:111]
	s_and_b64 vcc, exec, vcc
	v_mfma_f32_32x32x16_bf16 v[96:111], v[6:9], v[128:131], v[96:111]
	v_mfma_f32_32x32x16_bf16 v[112:127], v[10:13], v[132:135], v[112:127]
	v_mfma_f32_32x32x16_bf16 v[96:111], v[186:189], v[132:135], v[96:111]
	v_mfma_f32_32x32x16_bf16 v[112:127], v[170:173], v[136:139], v[112:127]
	v_mfma_f32_32x32x16_bf16 v[96:111], v[174:177], v[136:139], v[96:111]
	v_mfma_f32_32x32x16_bf16 v[112:127], v[178:181], v[140:143], v[112:127]
	v_mfma_f32_32x32x16_bf16 v[96:111], v[182:185], v[140:143], v[96:111]
	s_cbranch_vccnz .LBB0_837
	v_add_u32_e32 v0, 0, v159
	v_add_u32_e32 v2, 0x207fc, v0
	v_add_u32_e32 v4, 0x2087c, v0
	ds_read2_b32 v[2:3], v2 offset1:1
	ds_read2_b32 v[4:5], v4 offset1:1
	v_add_u32_e32 v6, 0x20804, v0
	v_add_u32_e32 v8, 0x20884, v0
	v_add_u32_e32 v10, 0x2081c, v0
	v_add_u32_e32 v12, 0x2089c, v0
	v_add_u32_e32 v14, 0x20824, v0
	v_add_u32_e32 v166, 0x208a4, v0
	v_add_u32_e32 v168, 0x2083c, v0
	v_add_u32_e32 v170, 0x208bc, v0
	v_add_u32_e32 v172, 0x20844, v0
	v_add_u32_e32 v174, 0x208c4, v0
	v_add_u32_e32 v176, 0x2085c, v0
	v_add_u32_e32 v178, 0x208dc, v0
	v_add_u32_e32 v180, 0x20864, v0
	v_add_u32_e32 v0, 0x208e4, v0
	ds_read2_b32 v[6:7], v6 offset1:1
	ds_read2_b32 v[8:9], v8 offset1:1
	ds_read2_b32 v[10:11], v10 offset1:1
	ds_read2_b32 v[12:13], v12 offset1:1
	ds_read2_b32 v[14:15], v14 offset1:1
	ds_read2_b32 v[166:167], v166 offset1:1
	ds_read2_b32 v[168:169], v168 offset1:1
	ds_read2_b32 v[170:171], v170 offset1:1
	ds_read2_b32 v[172:173], v172 offset1:1
	ds_read2_b32 v[174:175], v174 offset1:1
	ds_read2_b32 v[176:177], v176 offset1:1
	ds_read2_b32 v[178:179], v178 offset1:1
	ds_read2_b32 v[180:181], v180 offset1:1
	s_waitcnt lgkmcnt(0)
	v_pk_add_f32 v[112:113], v[112:113], v[2:3]
	ds_read2_b32 v[2:3], v0 offset1:1
	v_pk_add_f32 v[124:125], v[124:125], v[176:177]
	v_pk_add_f32 v[122:123], v[122:123], v[172:173]
	v_pk_add_f32 v[126:127], v[126:127], v[180:181]
	v_pk_add_f32 v[120:121], v[120:121], v[168:169]
	v_pk_add_f32 v[118:119], v[118:119], v[14:15]
	v_pk_add_f32 v[116:117], v[116:117], v[10:11]
	v_pk_add_f32 v[114:115], v[114:115], v[6:7]
	s_waitcnt lgkmcnt(0)
	v_pk_add_f32 v[110:111], v[110:111], v[2:3]
	v_pk_add_f32 v[108:109], v[108:109], v[178:179]
	v_pk_add_f32 v[106:107], v[106:107], v[174:175]
	v_pk_add_f32 v[104:105], v[104:105], v[170:171]
	v_pk_add_f32 v[102:103], v[102:103], v[166:167]
	v_pk_add_f32 v[100:101], v[100:101], v[12:13]
	v_pk_add_f32 v[98:99], v[98:99], v[8:9]
	v_pk_add_f32 v[96:97], v[96:97], v[4:5]

; #define MFMA32(a, b, c) __builtin_amdgcn_mfma_f32_32x32x16_bf16((a), (b), (c), 0, 0, 0)
; template <int OFF> DI s16x4 at_tr_read(int vb) { s16x4 r; asm volatile("ds_read_b64_tr_b16 %0, %1 offset:%2" : "=&v"(r) : "v"(vb), "i"(OFF) : "memory"); return r; }
; DI unsigned at_cvtpk(float lo, float hi) { unsigned r; asm volatile("v_cvt_pk_bf16_f32 %0, %1, %2" : "=v"(r) : "v"(lo), "v"(hi)); return r; }
; DI float at_softmax(f32x16& p0, f32x16& p1, float& m_run, bool first, bool nearb, LAS const float* tabp, int lane) {
;     ...
;     for (int i = 0; i < 16; ++i) p0[i] = __builtin_amdgcn_exp2f(p0[i]);
; #pragma unroll
;     for (int i = 0; i < 16; ++i) p1[i] = __builtin_amdgcn_exp2f(p1[i]);
;     return alpha;
; }
; DI bf16x8 at_pack(const f32x16& p, int s8) {
;     u32x4 w; w.x = at_cvtpk(p[s8], p[s8 + 1]); w.y = at_cvtpk(p[s8 + 2], p[s8 + 3]); w.z = at_cvtpk(p[s8 + 4], p[s8 + 5]); w.w = at_cvtpk(p[s8 + 6], p[s8 + 7]);
;     return __builtin_bit_cast(bf16x8, w);
; }
; template <int D0> DI void at_pv_block(f32x16 (&o)[4], int vb, const bf16x8 (&pf)[4]) {
;     const s16x4 l0 = at_tr_read<D0 * 512 + 0 * 4096>(vb), h0 = at_tr_read<D0 * 512 + 0 * 4096 + 2048>(vb), l1 = at_tr_read<D0 * 512 + 1 * 4096>(vb), h1 = at_tr_read<D0 * 512 + 1 * 4096 + 2048>(vb);
;     const s16x4 l2 = at_tr_read<D0 * 512 + 2 * 4096>(vb), h2 = at_tr_read<D0 * 512 + 2 * 4096 + 2048>(vb), l3 = at_tr_read<D0 * 512 + 3 * 4096>(vb), h3 = at_tr_read<D0 * 512 + 3 * 4096 + 2048>(vb);
;     asm volatile("s_waitcnt lgkmcnt(0)" ::: "memory"); __builtin_amdgcn_sched_barrier(0);
;     ...
;     o[D0] = MFMA32(AT_PK(l0, h0), pf[0], o[D0]); o[D0] = MFMA32(AT_PK(l1, h1), pf[1], o[D0]); o[D0] = MFMA32(AT_PK(l2, h2), pf[2], o[D0]); o[D0] = MFMA32(AT_PK(l3, h3), pf[3], o[D0]);
; DI void attn_unit_diff(const Ctx& C, int l, int b, int h, int j) {
;     ...
;             pf[0] = at_pack(p0, 0); pf[1] = at_pack(p0, 8); pf[2] = at_pack(p1, 0); pf[3] = at_pack(p1, 8);
;             ol = MFMA32(ones, pf[0], ol); ol = MFMA32(ones, pf[1], ol); ol = MFMA32(ones, pf[2], ol); ol = MFMA32(ones, pf[3], ol);
;             at_pv_block<0>(o, vb, pf); at_pv_block<1>(o, vb, pf); at_pv_block<2>(o, vb, pf); at_pv_block<3>(o, vb, pf);
.LBB0_844:
	v_subrev_u32_e32 v87, s48, v160
	v_add_u32_e32 v87, s31, v87
	ds_read_b64_tr_b16 v[170:171], v87 offset:0x0
	ds_read_b64_tr_b16 v[172:173], v87 offset:0x800
	ds_read_b64_tr_b16 v[174:175], v87 offset:0x200
	ds_read_b64_tr_b16 v[176:177], v87 offset:0xa00
	ds_read_b64_tr_b16 v[178:179], v87 offset:0x400
	ds_read_b64_tr_b16 v[180:181], v87 offset:0xc00
	ds_read_b64_tr_b16 v[182:183], v87 offset:0x600
	ds_read_b64_tr_b16 v[184:185], v87 offset:0xe00
	v_exp_f32_e32 v112, v112
	v_exp_f32_e32 v113, v113
	v_exp_f32_e32 v114, v114
	v_exp_f32_e32 v115, v115
	v_exp_f32_e32 v116, v116
	v_exp_f32_e32 v117, v117
	v_exp_f32_e32 v118, v118
	v_exp_f32_e32 v119, v119
	v_cvt_pk_bf16_f32 v2, v112, v113
	v_cvt_pk_bf16_f32 v3, v114, v115
	v_cvt_pk_bf16_f32 v4, v116, v117
	v_cvt_pk_bf16_f32 v5, v118, v119
	v_add_f32_e32 v81, v112, v113
	v_add_f32_e32 v82, v114, v115
	v_add_f32_e32 v83, v116, v117
	v_add_f32_e32 v84, v118, v119
	v_add_f32_e32 v81, v81, v82
	v_add_f32_e32 v83, v83, v84
	v_add_f32_e32 v81, v81, v83
	v_add_f32_e32 v80, v80, v81
	s_waitcnt lgkmcnt(0)
	ds_read_b64_tr_b16 v[112:113], v87 offset:0x1000
	ds_read_b64_tr_b16 v[114:115], v87 offset:0x1800
	ds_read_b64_tr_b16 v[116:117], v87 offset:0x1200
	ds_read_b64_tr_b16 v[118:119], v87 offset:0x1a00
	ds_read_b64_tr_b16 v[88:89], v87 offset:0x1400
	ds_read_b64_tr_b16 v[90:91], v87 offset:0x1c00
	ds_read_b64_tr_b16 v[92:93], v87 offset:0x1600
	ds_read_b64_tr_b16 v[94:95], v87 offset:0x1e00
	v_mfma_f32_32x32x16_bf16 v[64:79], v[170:173], v[2:5], v[64:79]
	v_exp_f32_e32 v120, v120
	v_exp_f32_e32 v121, v121
	v_mfma_f32_32x32x16_bf16 v[48:63], v[174:177], v[2:5], v[48:63]
	v_exp_f32_e32 v122, v122
	v_exp_f32_e32 v123, v123
	v_mfma_f32_32x32x16_bf16 v[32:47], v[178:181], v[2:5], v[32:47]
	v_exp_f32_e32 v124, v124
	v_exp_f32_e32 v125, v125
	v_mfma_f32_32x32x16_bf16 v[16:31], v[182:185], v[2:5], v[16:31]
	v_exp_f32_e32 v126, v126
	v_exp_f32_e32 v127, v127
	v_cvt_pk_bf16_f32 v6, v120, v121
	v_cvt_pk_bf16_f32 v7, v122, v123
	v_cvt_pk_bf16_f32 v8, v124, v125
	v_cvt_pk_bf16_f32 v9, v126, v127
	v_add_f32_e32 v81, v120, v121
	v_add_f32_e32 v82, v122, v123
	v_add_f32_e32 v83, v124, v125
	v_add_f32_e32 v84, v126, v127
	v_add_f32_e32 v81, v81, v82
	v_add_f32_e32 v83, v83, v84
	v_add_f32_e32 v81, v81, v83
	v_add_f32_e32 v80, v80, v81
	s_waitcnt lgkmcnt(0)
	ds_read_b64_tr_b16 v[170:171], v87 offset:0x2000
	ds_read_b64_tr_b16 v[172:173], v87 offset:0x2800
	ds_read_b64_tr_b16 v[174:175], v87 offset:0x2200
	ds_read_b64_tr_b16 v[176:177], v87 offset:0x2a00
	ds_read_b64_tr_b16 v[178:179], v87 offset:0x2400
	ds_read_b64_tr_b16 v[180:181], v87 offset:0x2c00
	ds_read_b64_tr_b16 v[182:183], v87 offset:0x2600
	ds_read_b64_tr_b16 v[184:185], v87 offset:0x2e00
	v_mfma_f32_32x32x16_bf16 v[64:79], v[112:115], v[6:9], v[64:79]
	v_exp_f32_e32 v96, v96
	v_exp_f32_e32 v97, v97
	v_mfma_f32_32x32x16_bf16 v[48:63], v[116:119], v[6:9], v[48:63]
	v_exp_f32_e32 v98, v98
	v_exp_f32_e32 v99, v99
	v_mfma_f32_32x32x16_bf16 v[32:47], v[88:91], v[6:9], v[32:47]
	v_exp_f32_e32 v100, v100
	v_exp_f32_e32 v101, v101
	v_mfma_f32_32x32x16_bf16 v[16:31], v[92:95], v[6:9], v[16:31]
	v_exp_f32_e32 v102, v102
	v_exp_f32_e32 v103, v103
	v_cvt_pk_bf16_f32 v10, v96, v97
	v_cvt_pk_bf16_f32 v11, v98, v99
	v_cvt_pk_bf16_f32 v12, v100, v101
	v_cvt_pk_bf16_f32 v13, v102, v103
	v_add_f32_e32 v81, v96, v97
	v_add_f32_e32 v82, v98, v99
	v_add_f32_e32 v83, v100, v101
	v_add_f32_e32 v84, v102, v103
	v_add_f32_e32 v81, v81, v82
	v_add_f32_e32 v83, v83, v84
	v_add_f32_e32 v81, v81, v83
	v_add_f32_e32 v80, v80, v81
	s_waitcnt lgkmcnt(0)
	ds_read_b64_tr_b16 v[112:113], v87 offset:0x3000
	ds_read_b64_tr_b16 v[114:115], v87 offset:0x3800
	ds_read_b64_tr_b16 v[116:117], v87 offset:0x3200
	ds_read_b64_tr_b16 v[118:119], v87 offset:0x3a00
	ds_read_b64_tr_b16 v[88:89], v87 offset:0x3400
	ds_read_b64_tr_b16 v[90:91], v87 offset:0x3c00
	ds_read_b64_tr_b16 v[92:93], v87 offset:0x3600
	ds_read_b64_tr_b16 v[94:95], v87 offset:0x3e00
	v_mfma_f32_32x32x16_bf16 v[64:79], v[170:173], v[10:13], v[64:79]
	v_exp_f32_e32 v104, v104
	v_exp_f32_e32 v105, v105
	v_mfma_f32_32x32x16_bf16 v[48:63], v[174:177], v[10:13], v[48:63]
	v_exp_f32_e32 v106, v106
	v_exp_f32_e32 v107, v107
	v_mfma_f32_32x32x16_bf16 v[32:47], v[178:181], v[10:13], v[32:47]
	v_exp_f32_e32 v108, v108
	v_exp_f32_e32 v109, v109
	v_mfma_f32_32x32x16_bf16 v[16:31], v[182:185], v[10:13], v[16:31]
	v_exp_f32_e32 v110, v110
	v_exp_f32_e32 v111, v111
	v_cvt_pk_bf16_f32 v166, v104, v105
	v_cvt_pk_bf16_f32 v167, v106, v107
	v_cvt_pk_bf16_f32 v168, v108, v109
	v_cvt_pk_bf16_f32 v169, v110, v111
	v_add_f32_e32 v81, v104, v105
	v_add_f32_e32 v82, v106, v107
	v_add_f32_e32 v83, v108, v109
	v_add_f32_e32 v84, v110, v111
	v_add_f32_e32 v81, v81, v82
	v_add_f32_e32 v83, v83, v84
	v_add_f32_e32 v81, v81, v83
	v_add_f32_e32 v80, v80, v81
	s_waitcnt lgkmcnt(0)
	s_mov_b64 s[42:43], 0
	s_mov_b64 s[58:59], -1
	s_and_b64 vcc, exec, s[76:77]
	s_cbranch_vccz .LBB0_833

; #define LAS __attribute__((address_space(3)))
; #define CIN(i) ((const float*)*(const GAS float* const __attribute__((address_space(4)))*)(C.ka + 8 * (i)))
; DI void attn_unit_diff(const Ctx& C, int l, int b, int h, int j) {
;     ...
;     const float inv = 1.f / ol[0];
;     LAS float* cmb = (LAS float*)C.lds + (size_t)wq * (64 * 64);
;     f32x4 sgv[4][4];
;     if (g == 0) { const float* sg0 = CIN(I_SUBLN) + l * 128;
; #pragma unroll
;         for (int d0 = 0; d0 < 4; ++d0)
; #pragma unroll
;             for (int gq = 0; gq < 4; ++gq) sgv[d0][gq] = *(const f32x4*)(sg0 + 32 * d0 + 8 * gq + 4 * hi); }
.LBB0_848:
	v_mfma_f32_32x32x16_bf16 v[64:79], v[112:115], v[166:169], v[64:79]
	v_mfma_f32_32x32x16_bf16 v[48:63], v[116:119], v[166:169], v[48:63]
	v_mfma_f32_32x32x16_bf16 v[32:47], v[88:91], v[166:169], v[32:47]
	v_mfma_f32_32x32x16_bf16 v[16:31], v[92:95], v[166:169], v[16:31]
	s_nop 15
v_lshlrev_b32_e32 v81, 2, v154
v_xor_b32_e32 v81, 0x80, v81
ds_bpermute_b32 v82, v81, v80
s_waitcnt lgkmcnt(0)
v_add_f32_e32 v80, v80, v82
	v_readlane_b32 s6, v252, 27
	v_readlane_b32 s7, v252, 28
	s_and_b64 vcc, s[6:7], exec
	s_cbranch_vccz .LBB0_850
	s_load_dwordx2 s[6:7], s[0:1], 0x38
	v_readlane_b32 s42, v254, 25
	v_readlane_b32 s43, v254, 26
	s_lshl_b64 s[42:43], s[42:43], 2
	v_lshlrev_b32_e32 v2, 2, v156
	s_waitcnt lgkmcnt(0)
	s_add_u32 s6, s6, s42
	v_ashrrev_i32_e32 v3, 31, v2
	s_addc_u32 s7, s7, s43
	v_lshl_add_u64 v[2:3], v[2:3], 2, s[6:7]
	global_load_dwordx4 v[126:129], v[2:3], off
	global_load_dwordx4 v[94:97], v[2:3], off offset:32
	global_load_dwordx4 v[86:89], v[2:3], off offset:64
	global_load_dwordx4 v[82:85], v[2:3], off offset:96
	global_load_dwordx4 v[90:93], v[2:3], off offset:128
	global_load_dwordx4 v[98:101], v[2:3], off offset:160
	global_load_dwordx4 v[102:105], v[2:3], off offset:192
	global_load_dwordx4 v[106:109], v[2:3], off offset:224
	global_load_dwordx4 v[110:113], v[2:3], off offset:256
	global_load_dwordx4 v[114:117], v[2:3], off offset:288
	global_load_dwordx4 v[118:121], v[2:3], off offset:320
	global_load_dwordx4 v[122:125], v[2:3], off offset:352
	global_load_dwordx4 v[130:133], v[2:3], off offset:384
	global_load_dwordx4 v[10:13], v[2:3], off offset:416
	global_load_dwordx4 v[6:9], v[2:3], off offset:448
	s_nop 0
	global_load_dwordx4 v[2:5], v[2:3], off offset:480
